# v18_mul24
# baseline (speedup 1.0000x reference)
.LBB1_101:
	v_add_u32_e32 v68, 0x1cac0, v67
	v_add_u32_e32 v69, 0x1cad0, v67
	v_add_u32_e32 v70, 0x1cae0, v67
	v_add_u32_e32 v71, 0x1caf0, v67
	ds_read_b32 v68, v68
	ds_read_b32 v72, v66
	ds_read_b32 v73, v66 offset:1088
	ds_read_b32 v163, v66 offset:2176
	ds_read_b32 v164, v66 offset:3264
	ds_read_b32 v69, v69
	ds_read_b32 v70, v70
	ds_read_b32 v71, v71
	s_waitcnt lgkmcnt(6)
	v_mfma_f32_16x16x4_f32 a[0:3], v68, v72, a[0:3]
	s_add_i32 s55, s55, 1
	v_add_u32_e32 v67, 64, v67
	s_cmp_lt_i32 s55, s54
	v_add_u32_e32 v66, 0x1100, v66
	s_waitcnt lgkmcnt(2)
	v_mfma_f32_16x16x4_f32 a[0:3], v69, v73, a[0:3]
	s_waitcnt lgkmcnt(1)
	v_mfma_f32_16x16x4_f32 a[0:3], v70, v163, a[0:3]
	s_waitcnt lgkmcnt(0)
	v_mfma_f32_16x16x4_f32 a[0:3], v71, v164, a[0:3]
	s_cbranch_scc1 .LBB1_101
	s_lshl_b32 s55, s54, 4
	v_or_b32_e32 v66, s55, v131
	v_mul_u32_u24_e32 v66, s95, v66
	s_lshl_b32 s54, s54, 6
	v_add3_u32 v66, s54, v66, v129
	ds_read_b128 v[66:69], v66
	s_waitcnt lgkmcnt(0)
	s_nop 1
	v_mfma_f32_16x16x4_f32 a[4:7], v66, a0, 0
	v_or_b32_e32 v66, s55, v130
	v_mfma_f32_16x16x4_f32 a[4:7], v67, a1, a[4:7]
	v_mad_u64_u32 v[66:67], s[54:55], v66, s95, v[106:107]
	v_mfma_f32_16x16x4_f32 a[4:7], v68, a2, a[4:7]
	v_mfma_f32_16x16x4_f32 a[0:3], v69, a3, a[4:7]
	s_nop 9
	v_accvgpr_read_b32 v67, a0
	v_accvgpr_read_b32 v68, a1
	v_accvgpr_read_b32 v69, a2
	v_accvgpr_read_b32 v70, a3
	v_xor_b32_e32 v67, 0x80000000, v67
	v_xor_b32_e32 v68, 0x80000000, v68
	v_xor_b32_e32 v69, 0x80000000, v69
	v_xor_b32_e32 v70, 0x80000000, v70
	ds_write2_b32 v66, v67, v68 offset1:68
	ds_write2_b32 v66, v69, v70 offset0:136 offset1:204

.LBB1_104:
	s_lshl_b32 s96, s59, 4
	v_or_b32_e32 v164, s96, v131
	s_andn2_b64 vcc, exec, s[54:55]
	v_lshlrev_b32_e32 v163, 2, v164
	s_cbranch_vccnz .LBB1_114
	v_or_b32_e32 v66, s96, v130
	v_mul_u32_u24_e32 v165, s95, v66
	v_add3_u32 v68, v163, v165, s85
	s_cmp_eq_u32 s59, 0
	s_cbranch_scc1 .Lp1_lds_1
	v_accvgpr_read_b32 v66, a0
	v_accvgpr_read_b32 v67, a1
	v_accvgpr_read_b32 v68, a2
	v_accvgpr_read_b32 v69, a3
	s_branch .Lp1_go_1

.Lp1_fast_1:
	s_add_i32 s84, s84, 1
	v_add_u32_e32 v162, 0x1100, v162
	v_add_u32_e32 v161, 0x1140, v161
	s_cmp_lg_u32 s56, 4
	v_add_u32_e32 v160, 0x1140, v160
	s_cbranch_scc0 .LBB1_125
	s_mov_b32 s59, s56
	s_mov_b64 s[54:55], -1
	s_lshl_b32 s96, s59, 4
	v_or_b32_e32 v164, s96, v131
	v_lshlrev_b32_e32 v163, 2, v164
	v_or_b32_e32 v66, s96, v130
	v_mul_u32_u24_e32 v165, s95, v66
	v_add3_u32 v68, v163, v165, s85
	v_accvgpr_read_b32 v66, a0
	v_accvgpr_read_b32 v67, a1
	v_accvgpr_read_b32 v68, a2
	v_accvgpr_read_b32 v69, a3

.LBB1_113:
	s_or_b64 exec, exec, s[54:55]
	s_waitcnt lgkmcnt(2)
	v_rsq_f32_e32 v167, v166
	v_mul_f32_e32 v166, 0.5, v166
	s_lshl_b32 s54, s96, 2
	v_add3_u32 v165, v128, s54, v165
	s_waitcnt lgkmcnt(1)
	v_mul_f32_e32 v168, v166, v167
	v_fma_f32 v168, -v167, v168, s58
	v_mul_f32_e32 v167, v167, v168
	v_mul_f32_e32 v166, v166, v167
	v_fma_f32 v166, -v167, v166, s58
	v_mul_f32_e32 v167, v167, v166
	ds_bpermute_b32 v166, v129, v167
	ds_bpermute_b32 v168, v142, v167
	s_add_i32 s54, s54, 0x1dc00
	s_waitcnt lgkmcnt(1)
	v_mul_f32_e32 v66, v66, v166
	v_mul_f32_e32 v70, v70, v166
	ds_bpermute_b32 v166, v143, v167
	ds_bpermute_b32 v167, v144, v167
	s_waitcnt lgkmcnt(2)
	v_mul_f32_e32 v71, v71, v168
	v_cndmask_b32_e64 v70, v70, 0, s[40:41]
	v_cndmask_b32_e64 v71, v71, 0, s[42:43]
	ds_write2_b32 v165, v70, v71 offset1:68
	s_waitcnt lgkmcnt(2)
	v_mul_f32_e32 v70, v72, v166
	s_waitcnt lgkmcnt(1)
	v_mul_f32_e32 v71, v73, v167
	v_cndmask_b32_e64 v70, v70, 0, s[44:45]
	v_cndmask_b32_e64 v71, v71, 0, s[50:51]
	v_mul_f32_e32 v67, v67, v168
	v_pk_mul_f32 v[68:69], v[68:69], v[166:167]
	ds_write2_b32 v165, v70, v71 offset0:136 offset1:204
	v_mul_u32_u24_e32 v70, s95, v164
	v_cndmask_b32_e64 v66, v66, 0, s[38:39]
	v_cndmask_b32_e64 v67, 0, v67, s[40:41]
	v_cndmask_b32_e64 v69, v69, 0, s[46:47]
	v_cndmask_b32_e64 v68, v68, 0, s[48:49]
	v_add3_u32 v70, s54, v70, v148
	ds_write_b128 v70, v[66:69]
.LBB1_114:
	s_sub_i32 s54, 3, s59
	s_cmp_ge_u32 s86, s54
	s_waitcnt lgkmcnt(0)
	s_barrier
	s_cbranch_scc1 .LBB1_116
	s_add_i32 s54, s59, s92
	s_lshl_b32 s54, s54, 4
	v_or_b32_e32 v66, s54, v131
	s_lshl_b32 s55, s96, 2
	v_mul_u32_u24_e32 v66, s95, v66
	v_add3_u32 v70, v159, s55, v66
	ds_read2_b32 v[66:67], v70 offset1:4
	v_mul_u32_u24_e32 v68, s95, v164
	v_add3_u32 v71, s55, v68, v130
	ds_read2_b32 v[68:69], v71 offset1:4
	ds_read2_b32 v[72:73], v71 offset0:8 offset1:12
	ds_read2_b32 v[70:71], v70 offset0:8 offset1:12
	v_or_b32_e32 v166, s54, v130
	v_mul_u32_u24_e32 v166, s95, v166
	v_add3_u32 v166, v163, v166, s85
	s_waitcnt lgkmcnt(2)
	v_mfma_f32_16x16x4_f32 a[0:3], v66, v68, 0
	v_mfma_f32_16x16x4_f32 a[0:3], v67, v69, a[0:3]
	s_waitcnt lgkmcnt(0)
	v_mfma_f32_16x16x4_f32 a[0:3], v70, v72, a[0:3]
	v_mfma_f32_16x16x4_f32 a[0:3], v71, v73, a[0:3]
	s_nop 9
	ds_write_b32 v166, a0
	ds_write_b32 v166, a1 offset:272
	ds_write_b32 v166, a2 offset:544
	ds_write_b32 v166, a3 offset:816

.LBB1_120:
	s_cmp_ge_u32 s59, s96
	s_cbranch_scc1 .LBB1_119
	v_lshl_or_b32 v68, s96, 4, v131
	v_mul_u32_u24_e32 v68, s95, v68
	s_mov_b32 s97, 0
	v_add_u32_e32 v68, v66, v68
	v_mov_b32_e32 v69, v161
	s_mov_b32 s98, 0
	s_branch .LBB1_123

.LBB1_222:
	v_add_u32_e32 v4, 0x186c0, v3
	v_add_u32_e32 v5, 0x186d0, v3
	v_add_u32_e32 v6, 0x186e0, v3
	v_add_u32_e32 v7, 0x186f0, v3
	ds_read_b32 v4, v4
	ds_read_b32 v8, v2
	ds_read_b32 v9, v2 offset:1088
	ds_read_b32 v13, v2 offset:2176
	ds_read_b32 v14, v2 offset:3264
	ds_read_b32 v5, v5
	ds_read_b32 v6, v6
	ds_read_b32 v7, v7
	s_waitcnt lgkmcnt(6)
	v_mfma_f32_16x16x4_f32 a[0:3], v4, v8, a[0:3]
	s_add_i32 s53, s53, 1
	v_add_u32_e32 v3, 64, v3
	s_cmp_lt_i32 s53, s52
	v_add_u32_e32 v2, 0x1100, v2
	s_waitcnt lgkmcnt(2)
	v_mfma_f32_16x16x4_f32 a[0:3], v5, v9, a[0:3]
	s_waitcnt lgkmcnt(1)
	v_mfma_f32_16x16x4_f32 a[0:3], v6, v13, a[0:3]
	s_waitcnt lgkmcnt(0)
	v_mfma_f32_16x16x4_f32 a[0:3], v7, v14, a[0:3]
	s_cbranch_scc1 .LBB1_222
	s_lshl_b32 s53, s52, 4
	v_or_b32_e32 v2, s53, v131
	v_mul_u32_u24_e32 v2, s57, v2
	s_lshl_b32 s52, s52, 6
	v_add3_u32 v2, s52, v2, v129
	ds_read_b128 v[2:5], v2
	s_waitcnt lgkmcnt(0)
	s_nop 1
	v_mfma_f32_16x16x4_f32 a[4:7], v2, a0, 0
	v_or_b32_e32 v2, s53, v130
	v_mfma_f32_16x16x4_f32 a[4:7], v3, a1, a[4:7]
	v_mad_u64_u32 v[2:3], s[52:53], v2, s57, v[106:107]
	v_mfma_f32_16x16x4_f32 a[4:7], v4, a2, a[4:7]
	v_mfma_f32_16x16x4_f32 a[0:3], v5, a3, a[4:7]
	s_nop 9
	v_accvgpr_read_b32 v3, a0
	v_accvgpr_read_b32 v4, a1
	v_accvgpr_read_b32 v5, a2
	v_accvgpr_read_b32 v6, a3
	v_xor_b32_e32 v3, 0x80000000, v3
	v_xor_b32_e32 v4, 0x80000000, v4
	v_xor_b32_e32 v5, 0x80000000, v5
	v_xor_b32_e32 v6, 0x80000000, v6
	ds_write2_b32 v2, v3, v4 offset1:68
	ds_write2_b32 v2, v5, v6 offset0:136 offset1:204

.LBB1_225:
	s_lshl_b32 s97, s59, 4
	v_or_b32_e32 v14, s97, v131
	s_andn2_b64 vcc, exec, s[52:53]
	v_lshlrev_b32_e32 v13, 2, v14
	s_cbranch_vccnz .LBB1_235
	v_or_b32_e32 v2, s97, v130
	v_mul_u32_u24_e32 v15, s57, v2
	v_add3_u32 v4, v13, v15, s95
	s_cmp_eq_u32 s59, 0
	s_cbranch_scc1 .Lp1_lds_2
	v_accvgpr_read_b32 v2, a0
	v_accvgpr_read_b32 v3, a1
	v_accvgpr_read_b32 v4, a2
	v_accvgpr_read_b32 v5, a3
	s_branch .Lp1_go_2

.Lp1_fast_2:
	s_add_i32 s94, s94, 1
	v_add_u32_e32 v145, 0x1100, v145
	v_add_u32_e32 v147, 0x1140, v147
	s_cmp_lg_u32 s56, 4
	v_add_u32_e32 v11, 0x1140, v11
	s_cbranch_scc0 .LBB1_246
	s_mov_b32 s59, s56
	s_mov_b64 s[52:53], -1
	s_lshl_b32 s97, s59, 4
	v_or_b32_e32 v14, s97, v131
	v_lshlrev_b32_e32 v13, 2, v14
	v_or_b32_e32 v2, s97, v130
	v_mul_u32_u24_e32 v15, s57, v2
	v_add3_u32 v4, v13, v15, s95
	v_accvgpr_read_b32 v2, a0
	v_accvgpr_read_b32 v3, a1
	v_accvgpr_read_b32 v4, a2
	v_accvgpr_read_b32 v5, a3

.LBB1_234:
	s_or_b64 exec, exec, s[52:53]
	s_waitcnt lgkmcnt(2)
	v_rsq_f32_e32 v17, v16
	v_mul_f32_e32 v16, 0.5, v16
	s_lshl_b32 s52, s97, 2
	v_add3_u32 v15, v128, s52, v15
	s_waitcnt lgkmcnt(1)
	v_mul_f32_e32 v18, v16, v17
	v_fma_f32 v18, -v17, v18, s58
	v_mul_f32_e32 v17, v17, v18
	v_mul_f32_e32 v16, v16, v17
	v_fma_f32 v16, -v17, v16, s58
	v_mul_f32_e32 v17, v17, v16
	ds_bpermute_b32 v16, v129, v17
	ds_bpermute_b32 v18, v142, v17
	s_add_i32 s52, s52, 0x19800
	s_waitcnt lgkmcnt(1)
	v_mul_f32_e32 v2, v2, v16
	v_mul_f32_e32 v6, v6, v16
	ds_bpermute_b32 v16, v143, v17
	ds_bpermute_b32 v17, v144, v17
	s_waitcnt lgkmcnt(2)
	v_mul_f32_e32 v7, v7, v18
	v_cndmask_b32_e64 v6, v6, 0, s[40:41]
	v_cndmask_b32_e64 v7, v7, 0, s[42:43]
	ds_write2_b32 v15, v6, v7 offset1:68
	s_waitcnt lgkmcnt(2)
	v_mul_f32_e32 v6, v8, v16
	s_waitcnt lgkmcnt(1)
	v_mul_f32_e32 v7, v9, v17
	v_cndmask_b32_e64 v6, v6, 0, s[44:45]
	v_cndmask_b32_e64 v7, v7, 0, s[50:51]
	v_mul_f32_e32 v3, v3, v18
	v_pk_mul_f32 v[4:5], v[4:5], v[16:17]
	ds_write2_b32 v15, v6, v7 offset0:136 offset1:204
	v_mul_u32_u24_e32 v6, s57, v14
	v_cndmask_b32_e64 v2, v2, 0, s[38:39]
	v_cndmask_b32_e64 v3, 0, v3, s[40:41]
	v_cndmask_b32_e64 v5, v5, 0, s[46:47]
	v_cndmask_b32_e64 v4, v4, 0, s[48:49]
	v_add3_u32 v6, s52, v6, v148
	ds_write_b128 v6, v[2:5]
.LBB1_235:
	s_sub_i32 s52, 3, s59
	s_cmp_ge_u32 s86, s52
	s_waitcnt lgkmcnt(0)
	s_barrier
	s_cbranch_scc1 .LBB1_237
	s_add_i32 s52, s59, s92
	s_lshl_b32 s52, s52, 4
	v_or_b32_e32 v2, s52, v131
	s_lshl_b32 s53, s97, 2
	v_mul_u32_u24_e32 v2, s57, v2
	v_add3_u32 v6, v10, s53, v2
	ds_read2_b32 v[2:3], v6 offset1:4
	v_mul_u32_u24_e32 v4, s57, v14
	v_add3_u32 v7, s53, v4, v130
	ds_read2_b32 v[4:5], v7 offset1:4
	ds_read2_b32 v[8:9], v7 offset0:8 offset1:12
	ds_read2_b32 v[6:7], v6 offset0:8 offset1:12
	v_or_b32_e32 v16, s52, v130
	v_mul_u32_u24_e32 v16, s57, v16
	v_add3_u32 v16, v13, v16, s95
	s_waitcnt lgkmcnt(2)
	v_mfma_f32_16x16x4_f32 a[0:3], v2, v4, 0
	v_mfma_f32_16x16x4_f32 a[0:3], v3, v5, a[0:3]
	s_waitcnt lgkmcnt(0)
	v_mfma_f32_16x16x4_f32 a[0:3], v6, v8, a[0:3]
	v_mfma_f32_16x16x4_f32 a[0:3], v7, v9, a[0:3]
	s_nop 9
	ds_write_b32 v16, a0
	ds_write_b32 v16, a1 offset:272
	ds_write_b32 v16, a2 offset:544
	ds_write_b32 v16, a3 offset:816

.LBB1_241:
	s_cmp_ge_u32 s59, s55
	s_cbranch_scc1 .LBB1_240
	v_lshl_or_b32 v4, s55, 4, v131
	v_mul_u32_u24_e32 v4, s57, v4
	s_mov_b32 s97, 0
	v_add_u32_e32 v4, v2, v4
	v_mov_b32_e32 v5, v147
	s_mov_b32 s98, 0
	s_branch .LBB1_244

.LBB1_292:
	v_add_u32_e32 v4, 0x1cac0, v3
	v_add_u32_e32 v5, 0x1cad0, v3
	v_add_u32_e32 v6, 0x1cae0, v3
	v_add_u32_e32 v7, 0x1caf0, v3
	ds_read_b32 v4, v4
	ds_read_b32 v8, v2
	ds_read_b32 v9, v2 offset:1088
	ds_read_b32 v41, v2 offset:2176
	ds_read_b32 v42, v2 offset:3264
	ds_read_b32 v5, v5
	ds_read_b32 v6, v6
	ds_read_b32 v7, v7
	s_waitcnt lgkmcnt(6)
	v_mfma_f32_16x16x4_f32 a[0:3], v4, v8, a[0:3]
	s_add_i32 s53, s53, 1
	v_add_u32_e32 v3, 64, v3
	s_cmp_lt_i32 s53, s52
	v_add_u32_e32 v2, 0x1100, v2
	s_waitcnt lgkmcnt(2)
	v_mfma_f32_16x16x4_f32 a[0:3], v5, v9, a[0:3]
	s_waitcnt lgkmcnt(1)
	v_mfma_f32_16x16x4_f32 a[0:3], v6, v41, a[0:3]
	s_waitcnt lgkmcnt(0)
	v_mfma_f32_16x16x4_f32 a[0:3], v7, v42, a[0:3]
	s_cbranch_scc1 .LBB1_292
	s_lshl_b32 s53, s52, 4
	v_or_b32_e32 v2, s53, v19
	v_mul_u32_u24_e32 v2, s78, v2
	s_lshl_b32 s52, s52, 6
	v_add3_u32 v2, s52, v2, v17
	ds_read_b128 v[2:5], v2
	s_waitcnt lgkmcnt(0)
	s_nop 1
	v_mfma_f32_16x16x4_f32 a[4:7], v2, a0, 0
	v_or_b32_e32 v2, s53, v18
	v_mfma_f32_16x16x4_f32 a[4:7], v3, a1, a[4:7]
	v_mad_u64_u32 v[2:3], s[52:53], v2, s78, v[10:11]
	v_mfma_f32_16x16x4_f32 a[4:7], v4, a2, a[4:7]
	v_mfma_f32_16x16x4_f32 a[0:3], v5, a3, a[4:7]
	s_nop 9
	v_accvgpr_read_b32 v3, a0
	v_accvgpr_read_b32 v4, a1
	v_accvgpr_read_b32 v5, a2
	v_accvgpr_read_b32 v6, a3
	v_xor_b32_e32 v3, 0x80000000, v3
	v_xor_b32_e32 v4, 0x80000000, v4
	v_xor_b32_e32 v5, 0x80000000, v5
	v_xor_b32_e32 v6, 0x80000000, v6
	ds_write2_b32 v2, v3, v4 offset1:68
	ds_write2_b32 v2, v5, v6 offset0:136 offset1:204

.LBB1_295:
	s_lshl_b32 s80, s79, 4
	v_or_b32_e32 v42, s80, v19
	s_andn2_b64 vcc, exec, s[52:53]
	v_lshlrev_b32_e32 v41, 2, v42
	s_cbranch_vccnz .LBB1_305
	v_or_b32_e32 v2, s80, v18
	v_mul_u32_u24_e32 v44, s78, v2
	v_add3_u32 v4, v41, v44, s69
	s_cmp_eq_u32 s79, 0
	s_cbranch_scc1 .Lp1_lds_3
	v_accvgpr_read_b32 v2, a0
	v_accvgpr_read_b32 v3, a1
	v_accvgpr_read_b32 v4, a2
	v_accvgpr_read_b32 v5, a3
	s_branch .Lp1_go_3

.Lp1_fast_3:
	s_add_i32 s68, s68, 1
	v_add_u32_e32 v40, 0x1100, v40
	v_add_u32_e32 v39, 0x1140, v39
	s_cmp_lg_u32 s52, 4
	v_add_u32_e32 v38, 0x1140, v38
	s_cbranch_scc0 .LBB1_316
	s_mov_b32 s79, s52
	s_mov_b64 s[52:53], -1
	s_lshl_b32 s80, s79, 4
	v_or_b32_e32 v42, s80, v19
	v_lshlrev_b32_e32 v41, 2, v42
	v_or_b32_e32 v2, s80, v18
	v_mul_u32_u24_e32 v44, s78, v2
	v_add3_u32 v4, v41, v44, s69
	v_accvgpr_read_b32 v2, a0
	v_accvgpr_read_b32 v3, a1
	v_accvgpr_read_b32 v4, a2
	v_accvgpr_read_b32 v5, a3

.LBB1_304:
	s_or_b64 exec, exec, s[52:53]
	s_waitcnt lgkmcnt(2)
	v_rsq_f32_e32 v54, v53
	v_mul_f32_e32 v53, 0.5, v53
	s_lshl_b32 s52, s80, 2
	v_add3_u32 v44, v16, s52, v44
	s_waitcnt lgkmcnt(1)
	v_mul_f32_e32 v55, v53, v54
	v_fma_f32 v55, -v54, v55, s65
	v_mul_f32_e32 v54, v54, v55
	v_mul_f32_e32 v53, v53, v54
	v_fma_f32 v53, -v54, v53, s65
	v_mul_f32_e32 v53, v54, v53
	ds_bpermute_b32 v54, v17, v53
	s_waitcnt lgkmcnt(1)
	ds_bpermute_b32 v56, v26, v53
	ds_bpermute_b32 v55, v29, v53
	s_add_i32 s52, s52, 0x1dc00
	s_waitcnt lgkmcnt(2)
	v_mul_f32_e32 v2, v2, v54
	v_mul_f32_e32 v6, v6, v54
	ds_bpermute_b32 v54, v28, v53
	s_waitcnt lgkmcnt(2)
	v_mul_f32_e32 v7, v7, v56
	v_cndmask_b32_e64 v6, v6, 0, s[38:39]
	v_cndmask_b32_e64 v7, v7, 0, s[40:41]
	ds_write2_b32 v44, v6, v7 offset1:68
	s_waitcnt lgkmcnt(1)
	v_mul_f32_e32 v6, v8, v54
	v_mul_f32_e32 v7, v9, v55
	v_cndmask_b32_e64 v6, v6, 0, s[42:43]
	v_cndmask_b32_e64 v7, v7, 0, s[48:49]
	v_mul_f32_e32 v3, v3, v56
	v_pk_mul_f32 v[4:5], v[4:5], v[54:55]
	ds_write2_b32 v44, v6, v7 offset0:136 offset1:204
	v_mul_u32_u24_e32 v6, s78, v42
	v_cndmask_b32_e64 v2, v2, 0, s[36:37]
	v_cndmask_b32_e64 v3, 0, v3, s[38:39]
	v_cndmask_b32_e64 v5, v5, 0, s[44:45]
	v_cndmask_b32_e64 v4, v4, 0, s[46:47]
	v_add3_u32 v6, s52, v6, v33
	ds_write_b128 v6, v[2:5]
.LBB1_305:
	s_sub_i32 s52, 3, s79
	s_cmp_ge_u32 s86, s52
	s_waitcnt lgkmcnt(0)
	s_barrier
	s_cbranch_scc1 .LBB1_307
	s_add_i32 s52, s79, s76
	s_lshl_b32 s52, s52, 4
	v_or_b32_e32 v2, s52, v19
	s_lshl_b32 s53, s80, 2
	v_mul_u32_u24_e32 v2, s78, v2
	v_add3_u32 v6, v1, s53, v2
	ds_read2_b32 v[2:3], v6 offset1:4
	v_mul_u32_u24_e32 v4, s78, v42
	v_add3_u32 v7, s53, v4, v18
	ds_read2_b32 v[4:5], v7 offset1:4
	ds_read2_b32 v[8:9], v7 offset0:8 offset1:12
	ds_read2_b32 v[6:7], v6 offset0:8 offset1:12
	v_or_b32_e32 v53, s52, v18
	v_mul_u32_u24_e32 v53, s78, v53
	v_add3_u32 v53, v41, v53, s69
	s_waitcnt lgkmcnt(2)
	v_mfma_f32_16x16x4_f32 a[0:3], v2, v4, 0
	v_mfma_f32_16x16x4_f32 a[0:3], v3, v5, a[0:3]
	s_waitcnt lgkmcnt(0)
	v_mfma_f32_16x16x4_f32 a[0:3], v6, v8, a[0:3]
	v_mfma_f32_16x16x4_f32 a[0:3], v7, v9, a[0:3]
	s_nop 9
	ds_write_b32 v53, a0
	ds_write_b32 v53, a1 offset:272
	ds_write_b32 v53, a2 offset:544
	ds_write_b32 v53, a3 offset:816

.LBB1_311:
	s_cmp_ge_u32 s79, s80
	s_cbranch_scc1 .LBB1_310
	v_lshl_or_b32 v4, s80, 4, v19
	v_mul_u32_u24_e32 v4, s78, v4
	s_mov_b32 s81, 0
	v_add_u32_e32 v4, v2, v4
	v_mov_b32_e32 v5, v39
	s_mov_b32 s82, 0
	s_branch .LBB1_314

.LBB1_333:
	v_add_u32_e32 v2, 0x186c0, v1
	v_add_u32_e32 v3, 0x186d0, v1
	v_add_u32_e32 v4, 0x186e0, v1
	v_add_u32_e32 v5, 0x186f0, v1
	ds_read_b32 v2, v2
	ds_read_b32 v6, v0
	ds_read_b32 v7, v0 offset:1088
	ds_read_b32 v14, v0 offset:2176
	ds_read_b32 v34, v0 offset:3264
	ds_read_b32 v3, v3
	ds_read_b32 v4, v4
	ds_read_b32 v5, v5
	s_waitcnt lgkmcnt(6)
	v_mfma_f32_16x16x4_f32 a[0:3], v2, v6, a[0:3]
	s_add_i32 s53, s53, 1
	v_add_u32_e32 v1, 64, v1
	s_cmp_lt_i32 s53, s52
	v_add_u32_e32 v0, 0x1100, v0
	s_waitcnt lgkmcnt(2)
	v_mfma_f32_16x16x4_f32 a[0:3], v3, v7, a[0:3]
	s_waitcnt lgkmcnt(1)
	v_mfma_f32_16x16x4_f32 a[0:3], v4, v14, a[0:3]
	s_waitcnt lgkmcnt(0)
	v_mfma_f32_16x16x4_f32 a[0:3], v5, v34, a[0:3]
	s_cbranch_scc1 .LBB1_333
	s_lshl_b32 s53, s52, 4
	v_or_b32_e32 v0, s53, v19
	v_mul_u32_u24_e32 v0, s64, v0
	s_lshl_b32 s52, s52, 6
	v_add3_u32 v0, s52, v0, v17
	ds_read_b128 v[0:3], v0
	s_waitcnt lgkmcnt(0)
	s_nop 1
	v_mfma_f32_16x16x4_f32 a[4:7], v0, a0, 0
	v_or_b32_e32 v0, s53, v18
	v_mfma_f32_16x16x4_f32 a[4:7], v1, a1, a[4:7]
	v_mad_u64_u32 v[0:1], s[52:53], v0, s64, v[10:11]
	v_mfma_f32_16x16x4_f32 a[4:7], v2, a2, a[4:7]
	v_mfma_f32_16x16x4_f32 a[0:3], v3, a3, a[4:7]
	s_nop 9
	v_accvgpr_read_b32 v1, a0
	v_accvgpr_read_b32 v2, a1
	v_accvgpr_read_b32 v3, a2
	v_accvgpr_read_b32 v4, a3
	v_xor_b32_e32 v1, 0x80000000, v1
	v_xor_b32_e32 v2, 0x80000000, v2
	v_xor_b32_e32 v3, 0x80000000, v3
	v_xor_b32_e32 v4, 0x80000000, v4
	ds_write2_b32 v0, v1, v2 offset1:68
	ds_write2_b32 v0, v3, v4 offset0:136 offset1:204

.LBB1_336:
	s_lshl_b32 s75, s74, 4
	v_or_b32_e32 v34, s75, v19
	s_andn2_b64 vcc, exec, s[52:53]
	v_lshlrev_b32_e32 v14, 2, v34
	s_cbranch_vccnz .LBB1_346
	v_or_b32_e32 v0, s75, v18
	v_mul_u32_u24_e32 v35, s64, v0
	v_add3_u32 v2, v14, v35, s72
	s_cmp_eq_u32 s74, 0
	s_cbranch_scc1 .Lp1_lds_4
	v_accvgpr_read_b32 v0, a0
	v_accvgpr_read_b32 v1, a1
	v_accvgpr_read_b32 v2, a2
	v_accvgpr_read_b32 v3, a3
	s_branch .Lp1_go_4

.Lp1_fast_4:
	s_add_i32 s65, s65, 1
	v_add_u32_e32 v30, 0x1100, v30
	v_add_u32_e32 v32, 0x1140, v32
	s_cmp_lg_u32 s52, 4
	v_add_u32_e32 v12, 0x1140, v12
	s_cbranch_scc0 .LBB1_357
	s_mov_b32 s74, s52
	s_mov_b64 s[52:53], -1
	s_lshl_b32 s75, s74, 4
	v_or_b32_e32 v34, s75, v19
	v_lshlrev_b32_e32 v14, 2, v34
	v_or_b32_e32 v0, s75, v18
	v_mul_u32_u24_e32 v35, s64, v0
	v_add3_u32 v2, v14, v35, s72
	v_accvgpr_read_b32 v0, a0
	v_accvgpr_read_b32 v1, a1
	v_accvgpr_read_b32 v2, a2
	v_accvgpr_read_b32 v3, a3

.LBB1_345:
	s_or_b64 exec, exec, s[52:53]
	s_waitcnt lgkmcnt(2)
	v_rsq_f32_e32 v37, v36
	v_mul_f32_e32 v36, 0.5, v36
	s_lshl_b32 s52, s75, 2
	v_add3_u32 v35, v16, s52, v35
	s_waitcnt lgkmcnt(1)
	v_mul_f32_e32 v43, v36, v37
	v_fma_f32 v43, -v37, v43, s73
	v_mul_f32_e32 v37, v37, v43
	v_mul_f32_e32 v36, v36, v37
	v_fma_f32 v36, -v37, v36, s73
	v_mul_f32_e32 v37, v37, v36
	ds_bpermute_b32 v36, v17, v37
	ds_bpermute_b32 v43, v26, v37
	s_add_i32 s52, s52, 0x19800
	s_waitcnt lgkmcnt(1)
	v_mul_f32_e32 v0, v0, v36
	v_mul_f32_e32 v4, v4, v36
	ds_bpermute_b32 v36, v28, v37
	ds_bpermute_b32 v37, v29, v37
	s_waitcnt lgkmcnt(2)
	v_mul_f32_e32 v5, v5, v43
	v_cndmask_b32_e64 v4, v4, 0, s[38:39]
	v_cndmask_b32_e64 v5, v5, 0, s[40:41]
	ds_write2_b32 v35, v4, v5 offset1:68
	s_waitcnt lgkmcnt(2)
	v_mul_f32_e32 v4, v6, v36
	s_waitcnt lgkmcnt(1)
	v_mul_f32_e32 v5, v7, v37
	v_cndmask_b32_e64 v4, v4, 0, s[42:43]
	v_cndmask_b32_e64 v5, v5, 0, s[48:49]
	v_mul_f32_e32 v1, v1, v43
	v_pk_mul_f32 v[2:3], v[2:3], v[36:37]
	ds_write2_b32 v35, v4, v5 offset0:136 offset1:204
	v_mul_u32_u24_e32 v4, s64, v34
	v_cndmask_b32_e64 v0, v0, 0, s[36:37]
	v_cndmask_b32_e64 v1, 0, v1, s[38:39]
	v_cndmask_b32_e64 v3, v3, 0, s[44:45]
	v_cndmask_b32_e64 v2, v2, 0, s[46:47]
	v_add3_u32 v4, s52, v4, v33
	ds_write_b128 v4, v[0:3]
.LBB1_346:
	s_sub_i32 s52, 3, s74
	s_cmp_ge_u32 s86, s52
	s_waitcnt lgkmcnt(0)
	s_barrier
	s_cbranch_scc1 .LBB1_348
	s_add_i32 s52, s74, s76
	s_lshl_b32 s52, s52, 4
	v_or_b32_e32 v0, s52, v19
	s_lshl_b32 s53, s75, 2
	v_mul_u32_u24_e32 v0, s64, v0
	v_add3_u32 v4, v8, s53, v0
	ds_read2_b32 v[0:1], v4 offset1:4
	v_mul_u32_u24_e32 v2, s64, v34
	v_add3_u32 v5, s53, v2, v18
	ds_read2_b32 v[2:3], v5 offset1:4
	ds_read2_b32 v[6:7], v5 offset0:8 offset1:12
	ds_read2_b32 v[4:5], v4 offset0:8 offset1:12
	v_or_b32_e32 v36, s52, v18
	v_mul_u32_u24_e32 v36, s64, v36
	v_add3_u32 v36, v14, v36, s72
	s_waitcnt lgkmcnt(2)
	v_mfma_f32_16x16x4_f32 a[0:3], v0, v2, 0
	v_mfma_f32_16x16x4_f32 a[0:3], v1, v3, a[0:3]
	s_waitcnt lgkmcnt(0)
	v_mfma_f32_16x16x4_f32 a[0:3], v4, v6, a[0:3]
	v_mfma_f32_16x16x4_f32 a[0:3], v5, v7, a[0:3]
	s_nop 9
	ds_write_b32 v36, a0
	ds_write_b32 v36, a1 offset:272
	ds_write_b32 v36, a2 offset:544
	ds_write_b32 v36, a3 offset:816

.LBB1_352:
	s_cmp_ge_u32 s74, s75
	s_cbranch_scc1 .LBB1_351
	v_lshl_or_b32 v2, s75, 4, v19
	v_mul_u32_u24_e32 v2, s64, v2
	s_mov_b32 s79, 0
	v_add_u32_e32 v2, v0, v2
	v_mov_b32_e32 v3, v32
	s_mov_b32 s80, 0
	s_branch .LBB1_355
